# RMSNorm1 row loop: the lane's gain chunks loaded once before the loop instead of seven dependent reloads per row
# speedup vs baseline: 1.0040x; 1.0040x over previous
; #define GAS __attribute__((address_space(1)))
; __device__ __forceinline__ unsigned pk2(float lo, float hi) { return f2bf(lo) | (f2bf(hi) << 16); }
; __device__ __forceinline__ void rms_row_to_bf16(const float* xrow, const float* g, bf16* orow, int lane) {
;     const GAS f32x4* xr = (const GAS f32x4*)xrow + lane; const GAS f32x4* gr = (const GAS f32x4*)g + lane;
;     f32x4 v[8]; float s = 0.f;
; #pragma unroll
;     for (int j = 0; j < 8; ++j) { v[j] = __builtin_nontemporal_load(xr + 64 * j); s += (v[j].x * v[j].x + v[j].y * v[j].y) + (v[j].z * v[j].z + v[j].w * v[j].w); }
;     const float rstd = __builtin_amdgcn_rsqf(wave_sum(s) * (1.f / DM) + NORM_EPS);
;     GAS v2u* o8 = (GAS v2u*)orow + lane;
; #pragma unroll
;     for (int j = 0; j < 8; ++j) { const f32x4 gg = gr[64 * j]; v2u w; w.x = pk2(v[j].x * rstd * gg.x, v[j].y * rstd * gg.y); w.y = pk2(v[j].z * rstd * gg.z, v[j].w * rstd * gg.w); o8[64 * j] = w; }
; }
; __global__ void __launch_bounds__(512, 2) hymba_fwd(Args args) {
;     ...
;         { const int q = (CVS_IN + CVS_OUT + NGW - 1) / NGW, x0 = gw * q, x1 = (x0 + q < CVS_IN + CVS_OUT) ? x0 + q : CVS_IN + CVS_OUT;
;           convert_small_range(args.w_in, args.w_out, BTIN, BTOUT, x0, x1, lds + wave * 8448, lane); }
;         for (int m = gw; m < SEQ; m += NGW) rms_row_to_bf16(args.x + (size_t)m * DM, args.norm1_g, XN + (size_t)m * DM, lane);
.LBB0_48:
	s_cmpk_gt_i32 s34, 0x1fff
	s_cbranch_scc1 .LBB0_51
	s_waitcnt vmcnt(23)
	v_mbcnt_lo_u32_b32 v2, -1, 0
	v_mbcnt_hi_u32_b32 v2, -1, v2
	v_and_b32_e32 v3, 64, v2
	v_add_u32_e32 v3, 64, v3
	s_waitcnt vmcnt(22)
	v_xor_b32_e32 v4, 1, v2
	v_cmp_lt_i32_e32 vcc, v4, v3
	v_ashrrev_i32_e32 v129, 31, v128
	v_lshlrev_b64 v[0:1], 4, v[128:129]
	v_cndmask_b32_e32 v4, v2, v4, vcc
	s_waitcnt vmcnt(13)
	v_lshlrev_b32_e32 v42, 2, v4
	v_xor_b32_e32 v4, 2, v2
	v_cmp_lt_i32_e32 vcc, v4, v3
	v_lshl_add_u64 v[28:29], s[38:39], 0, v[0:1]
	s_mov_b64 s[0:1], 0x1400
	v_cndmask_b32_e32 v4, v2, v4, vcc
	v_lshlrev_b32_e32 v43, 2, v4
	v_xor_b32_e32 v4, 4, v2
	v_cmp_lt_i32_e32 vcc, v4, v3
	v_lshl_add_u64 v[32:33], v[28:29], 0, s[0:1]
	s_mov_b64 s[0:1], 0x1800
	v_cndmask_b32_e32 v4, v2, v4, vcc
	s_waitcnt vmcnt(12)
	v_lshlrev_b32_e32 v44, 2, v4
	v_xor_b32_e32 v4, 8, v2
	v_cmp_lt_i32_e32 vcc, v4, v3
	v_lshl_add_u64 v[34:35], v[28:29], 0, s[0:1]
	s_mov_b64 s[0:1], 0x1c00
	v_cndmask_b32_e32 v4, v2, v4, vcc
	v_lshlrev_b32_e32 v45, 2, v4
	v_xor_b32_e32 v4, 16, v2
	v_cmp_lt_i32_e32 vcc, v4, v3
	s_ashr_i32 s35, s34, 31
	v_lshl_add_u64 v[36:37], v[28:29], 0, s[0:1]
	v_cndmask_b32_e32 v4, v2, v4, vcc
	v_lshlrev_b32_e32 v46, 2, v4
	v_xor_b32_e32 v4, 32, v2
	s_lshl_b64 s[0:1], s[34:35], 12
	v_cmp_lt_i32_e32 vcc, v4, v3
	s_add_u32 s0, s26, s0
	s_addc_u32 s1, s27, s1
	v_cndmask_b32_e32 v2, v2, v4, vcc
	v_lshlrev_b32_e32 v47, 2, v2
	v_lshl_add_u64 v[2:3], v[128:129], 3, s[0:1]
	s_mov_b64 s[0:1], 0x2000000
	s_mov_b32 s22, s91
	s_ashr_i32 s91, s90, 31
	v_lshl_add_u64 v[38:39], v[2:3], 0, s[0:1]
	s_lshl_b64 s[0:1], s[90:91], 12
	s_lshl_b64 s[20:21], s[34:35], 13
	s_add_u32 s20, s36, s20
	s_addc_u32 s21, s37, s21
	s_mov_b64 s[8:9], 0x1000
	v_lshl_add_u64 v[0:1], s[20:21], 0, v[0:1]
	v_lshl_add_u64 v[30:31], v[28:29], 0, s[8:9]
	v_lshl_add_u64 v[40:41], v[0:1], 0, s[8:9]
	s_lshl_b64 s[8:9], s[90:91], 13
	s_mov_b32 s91, s22
	s_waitcnt vmcnt(11)
	v_mov_b32_e32 v48, 0x358637bd
	s_movk_i32 s20, 0x7fff
	v_mov_b32_e32 v49, 1
	s_mov_b32 s21, s34
	global_load_dwordx4 v[208:211], v[28:29], off
	global_load_dwordx4 v[212:215], v[28:29], off offset:1024
	global_load_dwordx4 v[216:219], v[28:29], off offset:2048
	global_load_dwordx4 v[220:223], v[28:29], off offset:3072
	global_load_dwordx4 v[224:227], v[30:31], off
	global_load_dwordx4 v[228:231], v[32:33], off
	global_load_dwordx4 v[232:235], v[34:35], off
	global_load_dwordx4 v[236:239], v[36:37], off
.LBB0_50:
	global_load_dwordx4 v[50:53], v[40:41], off offset:-4096 nt
	global_load_dwordx4 v[24:27], v[40:41], off offset:-3072 nt
	global_load_dwordx4 v[20:23], v[40:41], off offset:-2048 nt
	global_load_dwordx4 v[12:15], v[40:41], off nt
	global_load_dwordx4 v[16:19], v[40:41], off offset:-1024 nt
	global_load_dwordx4 v[8:11], v[40:41], off offset:1024 nt
	global_load_dwordx4 v[0:3], v[40:41], off offset:3072 nt
	global_load_dwordx4 v[4:7], v[40:41], off offset:2048 nt
	s_add_i32 s21, s21, s90
	v_lshl_add_u64 v[40:41], v[40:41], 0, s[8:9]
	s_cmpk_gt_i32 s21, 0x1fff
	s_waitcnt vmcnt(7)
	v_mov_b32_e32 v60, v51
	s_waitcnt vmcnt(6)
	v_mov_b32_e32 v61, v25
	v_mov_b32_e32 v64, v53
	v_mov_b32_e32 v65, v27
	v_mov_b32_e32 v58, v50
	v_mov_b32_e32 v59, v24
	v_mov_b32_e32 v62, v52
	v_mov_b32_e32 v63, v26
	s_waitcnt vmcnt(5)
	v_pk_mul_f32 v[66:67], v[22:23], v[22:23]
	v_pk_mul_f32 v[68:69], v[20:21], v[20:21]
	v_mov_b32_e32 v82, v50
	v_mov_b32_e32 v83, v52
	s_waitcnt vmcnt(0)
	v_mov_b32_e32 v54, v208
	v_mov_b32_e32 v55, v209
	v_mov_b32_e32 v56, v210
	v_mov_b32_e32 v57, v211
	v_mov_b32_e32 v84, v54
	v_mov_b32_e32 v85, v56
	v_mov_b32_e32 v52, v51
	v_mov_b32_e32 v56, v55
	v_mov_b32_e32 v50, v24
	v_mov_b32_e32 v51, v26
	v_mov_b32_e32 v26, v25
	v_pk_mul_f32 v[24:25], v[60:61], v[60:61]
	v_pk_mul_f32 v[54:55], v[64:65], v[64:65]
	v_pk_mov_b32 v[60:61], v[68:69], v[66:67] op_sel:[1,0]
	v_mov_b32_e32 v69, v67
	v_pk_fma_f32 v[24:25], v[58:59], v[58:59], v[24:25]
	v_pk_fma_f32 v[54:55], v[62:63], v[62:63], v[54:55]
	v_mul_f32_e32 v70, v17, v17
	v_mul_f32_e32 v72, v19, v19
	v_pk_add_f32 v[58:59], v[60:61], v[68:69]
	v_pk_add_f32 v[24:25], v[24:25], v[54:55]
	v_mul_f32_e32 v79, v12, v12
	v_mul_f32_e32 v81, v13, v13
	v_mul_f32_e32 v86, v14, v14
	v_mul_f32_e32 v87, v15, v15
	v_pk_fma_f32 v[64:65], v[16:17], v[16:17], v[70:71] op_sel_hi:[1,1,0]
	v_pk_fma_f32 v[66:67], v[18:19], v[18:19], v[72:73] op_sel_hi:[1,1,0]
	v_pk_add_f32 v[54:55], v[58:59], v[58:59] op_sel:[0,1] op_sel_hi:[1,0]
	v_pk_add_f32 v[24:25], v[24:25], v[24:25] op_sel:[0,1] op_sel_hi:[1,0]
	v_pk_mul_f32 v[74:75], v[10:11], v[10:11]
	v_pk_mul_f32 v[76:77], v[8:9], v[8:9]
	v_mov_b32_e32 v65, v86
	v_mov_b32_e32 v67, v87
	v_mov_b32_e32 v55, v81
	v_mov_b32_e32 v25, v79
	v_pk_mov_b32 v[70:71], v[76:77], v[74:75] op_sel:[1,0]
	v_mov_b32_e32 v77, v75
	v_pk_add_f32 v[58:59], v[64:65], v[66:67]
	v_pk_add_f32 v[24:25], v[24:25], v[54:55]
	v_mul_f32_e32 v78, v5, v5
	v_mul_f32_e32 v80, v7, v7
	v_pk_add_f32 v[60:61], v[70:71], v[76:77]
	v_pk_add_f32 v[24:25], v[24:25], v[58:59]
	v_mul_f32_e32 v88, v0, v0
	v_mul_f32_e32 v89, v1, v1
	v_mul_f32_e32 v90, v2, v2
	v_mul_f32_e32 v91, v3, v3
	v_pk_fma_f32 v[72:73], v[4:5], v[4:5], v[78:79] op_sel_hi:[1,1,0]
	v_pk_fma_f32 v[74:75], v[6:7], v[6:7], v[80:81] op_sel_hi:[1,1,0]
	v_pk_add_f32 v[60:61], v[60:61], v[60:61] op_sel:[0,1] op_sel_hi:[1,0]
	v_pk_add_f32 v[24:25], v[24:25], v[24:25] op_sel:[0,1] op_sel_hi:[1,0]
	v_mov_b32_e32 v73, v90
	v_mov_b32_e32 v75, v91
	v_mov_b32_e32 v61, v89
	v_mov_b32_e32 v25, v88
	v_pk_add_f32 v[62:63], v[72:73], v[74:75]
	v_pk_add_f32 v[24:25], v[24:25], v[60:61]
	s_nop 0
	v_pk_add_f32 v[24:25], v[24:25], v[62:63]
	s_nop 0
	v_add_f32_e32 v24, v24, v25
	ds_bpermute_b32 v25, v42, v24
	s_waitcnt lgkmcnt(0)
; #define GAS __attribute__((address_space(1)))
; __device__ __forceinline__ unsigned pk2(float lo, float hi) { return f2bf(lo) | (f2bf(hi) << 16); }
; __device__ __forceinline__ void rms_row_to_bf16(const float* xrow, const float* g, bf16* orow, int lane) {
;     ...
;     for (int j = 0; j < 8; ++j) { v[j] = __builtin_nontemporal_load(xr + 64 * j); s += (v[j].x * v[j].x + v[j].y * v[j].y) + (v[j].z * v[j].z + v[j].w * v[j].w); }
;     const float rstd = __builtin_amdgcn_rsqf(wave_sum(s) * (1.f / DM) + NORM_EPS);
;     GAS v2u* o8 = (GAS v2u*)orow + lane;
; #pragma unroll
;     for (int j = 0; j < 8; ++j) { const f32x4 gg = gr[64 * j]; v2u w; w.x = pk2(v[j].x * rstd * gg.x, v[j].y * rstd * gg.y); w.y = pk2(v[j].z * rstd * gg.z, v[j].w * rstd * gg.w); o8[64 * j] = w; }
	v_add_f32_e32 v24, v24, v25
	ds_bpermute_b32 v25, v43, v24
	s_waitcnt lgkmcnt(0)
	v_add_f32_e32 v24, v24, v25
	ds_bpermute_b32 v25, v44, v24
	s_waitcnt lgkmcnt(0)
	v_add_f32_e32 v24, v24, v25
	ds_bpermute_b32 v25, v45, v24
	s_waitcnt lgkmcnt(0)
	v_add_f32_e32 v24, v24, v25
	ds_bpermute_b32 v25, v46, v24
	s_waitcnt lgkmcnt(0)
	v_add_f32_e32 v24, v24, v25
	ds_bpermute_b32 v25, v47, v24
	s_waitcnt lgkmcnt(0)
	v_add_f32_e32 v24, v24, v25
	v_fmamk_f32 v24, v24, 0x3a000000, v48
	v_rsq_f32_e32 v24, v24
	s_nop 0
	v_pk_mul_f32 v[54:55], v[82:83], v[24:25] op_sel_hi:[1,0]
	v_pk_mul_f32 v[52:53], v[52:53], v[24:25] op_sel_hi:[1,0]
	v_pk_mul_f32 v[58:59], v[50:51], v[24:25] op_sel_hi:[1,0]
	v_pk_mul_f32 v[50:51], v[84:85], v[54:55]
	v_pk_mul_f32 v[52:53], v[56:57], v[52:53]
	v_and_b32_sdwa v25, v51, v49 dst_sel:DWORD dst_unused:UNUSED_PAD src0_sel:WORD_1 src1_sel:DWORD
	v_and_b32_sdwa v55, v53, v49 dst_sel:DWORD dst_unused:UNUSED_PAD src0_sel:WORD_1 src1_sel:DWORD
	v_and_b32_sdwa v56, v52, v49 dst_sel:DWORD dst_unused:UNUSED_PAD src0_sel:WORD_1 src1_sel:DWORD
	v_and_b32_sdwa v54, v50, v49 dst_sel:DWORD dst_unused:UNUSED_PAD src0_sel:WORD_1 src1_sel:DWORD
	v_add3_u32 v25, v51, v25, s20
	v_add3_u32 v51, v53, v55, s20
	v_add3_u32 v52, v52, v56, s20
	v_add3_u32 v50, v50, v54, s20
	v_and_b32_e32 v51, 0xffff0000, v51
	v_and_b32_e32 v52, 0xffff0000, v52
	v_or_b32_sdwa v51, v51, v25 dst_sel:DWORD dst_unused:UNUSED_PAD src0_sel:DWORD src1_sel:WORD_1
	v_or_b32_sdwa v50, v52, v50 dst_sel:DWORD dst_unused:UNUSED_PAD src0_sel:DWORD src1_sel:WORD_1
	global_store_dwordx2 v[38:39], v[50:51], off
	s_nop 1
	v_mov_b32_e32 v50, v212
	v_mov_b32_e32 v51, v213
	v_mov_b32_e32 v52, v214
	v_mov_b32_e32 v53, v215
	v_pk_mul_f32 v[26:27], v[26:27], v[24:25] op_sel_hi:[1,0]
	v_mov_b32_e32 v55, v52
	v_mov_b32_e32 v52, v51
	v_mov_b32_e32 v54, v50
	v_pk_mul_f32 v[26:27], v[52:53], v[26:27]
	v_pk_mul_f32 v[50:51], v[54:55], v[58:59]
	v_and_b32_sdwa v53, v27, v49 dst_sel:DWORD dst_unused:UNUSED_PAD src0_sel:WORD_1 src1_sel:DWORD
	v_and_b32_sdwa v54, v26, v49 dst_sel:DWORD dst_unused:UNUSED_PAD src0_sel:WORD_1 src1_sel:DWORD
	v_and_b32_sdwa v25, v51, v49 dst_sel:DWORD dst_unused:UNUSED_PAD src0_sel:WORD_1 src1_sel:DWORD
	v_and_b32_sdwa v52, v50, v49 dst_sel:DWORD dst_unused:UNUSED_PAD src0_sel:WORD_1 src1_sel:DWORD
	v_add3_u32 v27, v27, v53, s20
	v_add3_u32 v26, v26, v54, s20
	v_add3_u32 v50, v50, v52, s20
	v_add3_u32 v25, v51, v25, s20
	v_and_b32_e32 v27, 0xffff0000, v27
	v_and_b32_e32 v26, 0xffff0000, v26
	v_or_b32_sdwa v27, v27, v25 dst_sel:DWORD dst_unused:UNUSED_PAD src0_sel:DWORD src1_sel:WORD_1
	v_or_b32_sdwa v26, v26, v50 dst_sel:DWORD dst_unused:UNUSED_PAD src0_sel:DWORD src1_sel:WORD_1
	global_store_dwordx2 v[38:39], v[26:27], off offset:512
	s_nop 1
	v_mov_b32_e32 v50, v216
	v_mov_b32_e32 v51, v217
	v_mov_b32_e32 v52, v218
	v_mov_b32_e32 v53, v219
	v_mov_b32_e32 v26, v20
	v_mov_b32_e32 v27, v22
	v_mov_b32_e32 v22, v21
	v_pk_mul_f32 v[20:21], v[26:27], v[24:25] op_sel_hi:[1,0]
	v_pk_mul_f32 v[22:23], v[22:23], v[24:25] op_sel_hi:[1,0]
	v_mov_b32_e32 v27, v52
	v_mov_b32_e32 v52, v51
	v_mov_b32_e32 v26, v50
	v_pk_mul_f32 v[22:23], v[52:53], v[22:23]
	v_pk_mul_f32 v[20:21], v[26:27], v[20:21]
	v_and_b32_sdwa v27, v23, v49 dst_sel:DWORD dst_unused:UNUSED_PAD src0_sel:WORD_1 src1_sel:DWORD
	v_and_b32_sdwa v50, v22, v49 dst_sel:DWORD dst_unused:UNUSED_PAD src0_sel:WORD_1 src1_sel:DWORD
	v_and_b32_sdwa v25, v21, v49 dst_sel:DWORD dst_unused:UNUSED_PAD src0_sel:WORD_1 src1_sel:DWORD
	v_and_b32_sdwa v26, v20, v49 dst_sel:DWORD dst_unused:UNUSED_PAD src0_sel:WORD_1 src1_sel:DWORD
	v_add3_u32 v23, v23, v27, s20
	v_add3_u32 v22, v22, v50, s20
	v_add3_u32 v20, v20, v26, s20
	v_add3_u32 v21, v21, v25, s20
	v_and_b32_e32 v23, 0xffff0000, v23
	v_and_b32_e32 v22, 0xffff0000, v22
	v_or_b32_sdwa v21, v23, v21 dst_sel:DWORD dst_unused:UNUSED_PAD src0_sel:DWORD src1_sel:WORD_1
	v_or_b32_sdwa v20, v22, v20 dst_sel:DWORD dst_unused:UNUSED_PAD src0_sel:DWORD src1_sel:WORD_1
	global_store_dwordx2 v[38:39], v[20:21], off offset:1024
	s_nop 1
	v_mov_b32_e32 v20, v220
	v_mov_b32_e32 v21, v221
	v_mov_b32_e32 v22, v222
	v_mov_b32_e32 v23, v223
	v_mov_b32_e32 v26, v16
	v_mov_b32_e32 v27, v18
	v_mov_b32_e32 v18, v17
	v_pk_mul_f32 v[16:17], v[26:27], v[24:25] op_sel_hi:[1,0]
	v_pk_mul_f32 v[18:19], v[18:19], v[24:25] op_sel_hi:[1,0]
	v_mov_b32_e32 v27, v22
	v_mov_b32_e32 v22, v21
	v_mov_b32_e32 v26, v20
	v_pk_mul_f32 v[18:19], v[18:19], v[22:23]
	v_pk_mul_f32 v[16:17], v[16:17], v[26:27]
	v_and_b32_sdwa v22, v19, v49 dst_sel:DWORD dst_unused:UNUSED_PAD src0_sel:WORD_1 src1_sel:DWORD
	v_and_b32_sdwa v23, v18, v49 dst_sel:DWORD dst_unused:UNUSED_PAD src0_sel:WORD_1 src1_sel:DWORD
	v_and_b32_sdwa v20, v17, v49 dst_sel:DWORD dst_unused:UNUSED_PAD src0_sel:WORD_1 src1_sel:DWORD
	v_and_b32_sdwa v21, v16, v49 dst_sel:DWORD dst_unused:UNUSED_PAD src0_sel:WORD_1 src1_sel:DWORD
	v_add3_u32 v19, v19, v22, s20
	v_add3_u32 v18, v18, v23, s20
	v_add3_u32 v16, v16, v21, s20
	v_add3_u32 v17, v17, v20, s20
	v_and_b32_e32 v19, 0xffff0000, v19
	v_and_b32_e32 v18, 0xffff0000, v18
	v_or_b32_sdwa v17, v19, v17 dst_sel:DWORD dst_unused:UNUSED_PAD src0_sel:DWORD src1_sel:WORD_1
; #define GAS __attribute__((address_space(1)))
; __device__ __forceinline__ unsigned pk2(float lo, float hi) { return f2bf(lo) | (f2bf(hi) << 16); }
; __device__ __forceinline__ void rms_row_to_bf16(const float* xrow, const float* g, bf16* orow, int lane) {
;     ...
;     GAS v2u* o8 = (GAS v2u*)orow + lane;
; #pragma unroll
;     for (int j = 0; j < 8; ++j) { const f32x4 gg = gr[64 * j]; v2u w; w.x = pk2(v[j].x * rstd * gg.x, v[j].y * rstd * gg.y); w.y = pk2(v[j].z * rstd * gg.z, v[j].w * rstd * gg.w); o8[64 * j] = w; }
; }
	v_or_b32_sdwa v16, v18, v16 dst_sel:DWORD dst_unused:UNUSED_PAD src0_sel:DWORD src1_sel:WORD_1
	global_store_dwordx2 v[38:39], v[16:17], off offset:1536
	s_nop 1
	v_mov_b32_e32 v16, v224
	v_mov_b32_e32 v17, v225
	v_mov_b32_e32 v18, v226
	v_mov_b32_e32 v19, v227
	v_mov_b32_e32 v20, v12
	v_mov_b32_e32 v21, v14
	v_mov_b32_e32 v14, v13
	v_pk_mul_f32 v[12:13], v[20:21], v[24:25] op_sel_hi:[1,0]
	v_pk_mul_f32 v[14:15], v[14:15], v[24:25] op_sel_hi:[1,0]
	v_mov_b32_e32 v21, v18
	v_mov_b32_e32 v18, v17
	v_mov_b32_e32 v20, v16
	v_pk_mul_f32 v[14:15], v[14:15], v[18:19]
	v_pk_mul_f32 v[12:13], v[12:13], v[20:21]
	v_and_b32_sdwa v18, v15, v49 dst_sel:DWORD dst_unused:UNUSED_PAD src0_sel:WORD_1 src1_sel:DWORD
	v_and_b32_sdwa v19, v14, v49 dst_sel:DWORD dst_unused:UNUSED_PAD src0_sel:WORD_1 src1_sel:DWORD
	v_and_b32_sdwa v16, v13, v49 dst_sel:DWORD dst_unused:UNUSED_PAD src0_sel:WORD_1 src1_sel:DWORD
	v_and_b32_sdwa v17, v12, v49 dst_sel:DWORD dst_unused:UNUSED_PAD src0_sel:WORD_1 src1_sel:DWORD
	v_add3_u32 v15, v15, v18, s20
	v_add3_u32 v14, v14, v19, s20
	v_add3_u32 v12, v12, v17, s20
	v_add3_u32 v13, v13, v16, s20
	v_and_b32_e32 v15, 0xffff0000, v15
	v_and_b32_e32 v14, 0xffff0000, v14
	v_or_b32_sdwa v13, v15, v13 dst_sel:DWORD dst_unused:UNUSED_PAD src0_sel:DWORD src1_sel:WORD_1
	v_or_b32_sdwa v12, v14, v12 dst_sel:DWORD dst_unused:UNUSED_PAD src0_sel:DWORD src1_sel:WORD_1
	global_store_dwordx2 v[38:39], v[12:13], off offset:2048
	s_nop 1
	v_mov_b32_e32 v12, v228
	v_mov_b32_e32 v13, v229
	v_mov_b32_e32 v14, v230
	v_mov_b32_e32 v15, v231
	v_mov_b32_e32 v16, v8
	v_mov_b32_e32 v17, v10
	v_mov_b32_e32 v10, v9
	v_pk_mul_f32 v[8:9], v[16:17], v[24:25] op_sel_hi:[1,0]
	v_pk_mul_f32 v[10:11], v[10:11], v[24:25] op_sel_hi:[1,0]
	v_mov_b32_e32 v17, v14
	v_mov_b32_e32 v14, v13
	v_mov_b32_e32 v16, v12
	v_pk_mul_f32 v[10:11], v[10:11], v[14:15]
	v_pk_mul_f32 v[8:9], v[8:9], v[16:17]
	v_and_b32_sdwa v14, v11, v49 dst_sel:DWORD dst_unused:UNUSED_PAD src0_sel:WORD_1 src1_sel:DWORD
	v_and_b32_sdwa v15, v10, v49 dst_sel:DWORD dst_unused:UNUSED_PAD src0_sel:WORD_1 src1_sel:DWORD
	v_and_b32_sdwa v12, v9, v49 dst_sel:DWORD dst_unused:UNUSED_PAD src0_sel:WORD_1 src1_sel:DWORD
	v_and_b32_sdwa v13, v8, v49 dst_sel:DWORD dst_unused:UNUSED_PAD src0_sel:WORD_1 src1_sel:DWORD
	v_add3_u32 v11, v11, v14, s20
	v_add3_u32 v10, v10, v15, s20
	v_add3_u32 v8, v8, v13, s20
	v_add3_u32 v9, v9, v12, s20
	v_and_b32_e32 v11, 0xffff0000, v11
	v_and_b32_e32 v10, 0xffff0000, v10
	v_or_b32_sdwa v9, v11, v9 dst_sel:DWORD dst_unused:UNUSED_PAD src0_sel:DWORD src1_sel:WORD_1
	v_or_b32_sdwa v8, v10, v8 dst_sel:DWORD dst_unused:UNUSED_PAD src0_sel:DWORD src1_sel:WORD_1
	global_store_dwordx2 v[38:39], v[8:9], off offset:2560
	s_nop 1
	v_mov_b32_e32 v8, v232
	v_mov_b32_e32 v9, v233
	v_mov_b32_e32 v10, v234
	v_mov_b32_e32 v11, v235
	v_mov_b32_e32 v12, v4
	v_mov_b32_e32 v13, v6
	v_mov_b32_e32 v6, v5
	v_pk_mul_f32 v[4:5], v[12:13], v[24:25] op_sel_hi:[1,0]
	v_pk_mul_f32 v[6:7], v[6:7], v[24:25] op_sel_hi:[1,0]
	v_mov_b32_e32 v13, v10
	v_mov_b32_e32 v10, v9
	v_mov_b32_e32 v12, v8
	v_pk_mul_f32 v[6:7], v[6:7], v[10:11]
	v_pk_mul_f32 v[4:5], v[4:5], v[12:13]
	v_and_b32_sdwa v10, v7, v49 dst_sel:DWORD dst_unused:UNUSED_PAD src0_sel:WORD_1 src1_sel:DWORD
	v_and_b32_sdwa v11, v6, v49 dst_sel:DWORD dst_unused:UNUSED_PAD src0_sel:WORD_1 src1_sel:DWORD
	v_and_b32_sdwa v8, v5, v49 dst_sel:DWORD dst_unused:UNUSED_PAD src0_sel:WORD_1 src1_sel:DWORD
	v_and_b32_sdwa v9, v4, v49 dst_sel:DWORD dst_unused:UNUSED_PAD src0_sel:WORD_1 src1_sel:DWORD
	v_add3_u32 v7, v7, v10, s20
	v_add3_u32 v6, v6, v11, s20
	v_add3_u32 v4, v4, v9, s20
	v_add3_u32 v5, v5, v8, s20
	v_and_b32_e32 v7, 0xffff0000, v7
	v_and_b32_e32 v6, 0xffff0000, v6
	v_or_b32_sdwa v5, v7, v5 dst_sel:DWORD dst_unused:UNUSED_PAD src0_sel:DWORD src1_sel:WORD_1
	v_or_b32_sdwa v4, v6, v4 dst_sel:DWORD dst_unused:UNUSED_PAD src0_sel:DWORD src1_sel:WORD_1
	global_store_dwordx2 v[38:39], v[4:5], off offset:3072
	s_nop 1
	v_mov_b32_e32 v4, v236
	v_mov_b32_e32 v5, v237
	v_mov_b32_e32 v6, v238
	v_mov_b32_e32 v7, v239
	v_mov_b32_e32 v8, v0
	v_mov_b32_e32 v9, v2
	v_mov_b32_e32 v2, v1
	v_pk_mul_f32 v[0:1], v[8:9], v[24:25] op_sel_hi:[1,0]
	v_pk_mul_f32 v[2:3], v[2:3], v[24:25] op_sel_hi:[1,0]
	v_mov_b32_e32 v9, v6
	v_mov_b32_e32 v6, v5
	v_mov_b32_e32 v8, v4
	v_pk_mul_f32 v[2:3], v[2:3], v[6:7]
	v_pk_mul_f32 v[0:1], v[0:1], v[8:9]
	v_and_b32_sdwa v6, v3, v49 dst_sel:DWORD dst_unused:UNUSED_PAD src0_sel:WORD_1 src1_sel:DWORD
	v_and_b32_sdwa v7, v2, v49 dst_sel:DWORD dst_unused:UNUSED_PAD src0_sel:WORD_1 src1_sel:DWORD
	v_and_b32_sdwa v4, v1, v49 dst_sel:DWORD dst_unused:UNUSED_PAD src0_sel:WORD_1 src1_sel:DWORD
	v_and_b32_sdwa v5, v0, v49 dst_sel:DWORD dst_unused:UNUSED_PAD src0_sel:WORD_1 src1_sel:DWORD
	v_add3_u32 v3, v3, v6, s20
	v_add3_u32 v2, v2, v7, s20
	v_add3_u32 v0, v0, v5, s20
	v_add3_u32 v1, v1, v4, s20
	v_and_b32_e32 v3, 0xffff0000, v3
	v_and_b32_e32 v2, 0xffff0000, v2
	v_or_b32_sdwa v1, v3, v1 dst_sel:DWORD dst_unused:UNUSED_PAD src0_sel:DWORD src1_sel:WORD_1
	v_or_b32_sdwa v0, v2, v0 dst_sel:DWORD dst_unused:UNUSED_PAD src0_sel:DWORD src1_sel:WORD_1
	global_store_dwordx2 v[38:39], v[0:1], off offset:3584
	v_lshl_add_u64 v[38:39], v[38:39], 0, s[0:1]
	s_cbranch_scc0 .LBB0_50
